# GEMM phases: the accumulator zeroing block that hipcc emits before the K-loop-runs branch is skipped when the loop runs (its preheader zeroes the same 128 registers again)
# speedup vs baseline: 1.0062x; 1.0062x over previous
; template <class Epi, class Sched, bool ALIGN_EPI = false, bool SP2 = false>
; __device__ __forceinline__ void gemm_phase(PG8_LAS unsigned char* lds, const Gemm g, const Sched& S, const Epi& E) {
;     ...
;         for (int t = 0; t < nt; t += 2) {
;             if constexpr (Epi::MIDK) { if (t == (nt >> 1)) E.mid(acc, cur, wr, wc, fr, fq); }
;             const bool last = (t == nt - 2);
;             const char* a1 = cA + (size_t)(t + 1) * kstep;
;             const char* a2 = last ? nA : cA + (size_t)(t + 2) * kstep; const char* b2 = last ? nB : cB + (size_t)(t + 2) * kstep;
;             const char* a3 = a2 + kstep; const char* b3 = b2 + kstep;
;     ...
;         for (int a = 0; a < 2; ++a)
; #pragma unroll
;             for (int b = 0; b < 2; ++b)
; #pragma unroll
;                 for (int m = 0; m < 4; ++m)
; #pragma unroll
;                     for (int n = 0; n < 2; ++n) acc[a][b][m][n] = (f32x4){0.f, 0.f, 0.f, 0.f};
;         cur = nxt; cA = nA; cB = nB; ++ui;
.LBB0_202:
	v_mov_b32_e32 v37, 0
	s_andn2_b64 vcc, exec, s[38:39]
	s_cbranch_vccz .Lzk_1
	v_mov_b32_e32 v36, v37
	v_mov_b32_e32 v35, v37
	v_mov_b32_e32 v34, v37
	v_mov_b32_e32 v41, v37
	v_mov_b32_e32 v40, v37
	v_mov_b32_e32 v39, v37
	v_mov_b32_e32 v38, v37
	v_mov_b32_e32 v53, v37
	v_mov_b32_e32 v52, v37
	v_mov_b32_e32 v51, v37
	v_mov_b32_e32 v50, v37
	v_mov_b32_e32 v57, v37
	v_mov_b32_e32 v56, v37
	v_mov_b32_e32 v55, v37
	v_mov_b32_e32 v54, v37
	v_mov_b32_e32 v69, v37
	v_mov_b32_e32 v68, v37
	v_mov_b32_e32 v67, v37
	v_mov_b32_e32 v66, v37
	v_mov_b32_e32 v73, v37
	v_mov_b32_e32 v72, v37
	v_mov_b32_e32 v71, v37
	v_mov_b32_e32 v70, v37
	v_mov_b32_e32 v85, v37
	v_mov_b32_e32 v84, v37
	v_mov_b32_e32 v83, v37
	v_mov_b32_e32 v82, v37
	v_mov_b32_e32 v89, v37
	v_mov_b32_e32 v88, v37
	v_mov_b32_e32 v87, v37
	v_mov_b32_e32 v86, v37
	v_mov_b32_e32 v161, v37
	v_mov_b32_e32 v160, v37
	v_mov_b32_e32 v159, v37
	v_mov_b32_e32 v158, v37
	v_mov_b32_e32 v157, v37
	v_mov_b32_e32 v156, v37
	v_mov_b32_e32 v155, v37
	v_mov_b32_e32 v154, v37
	v_mov_b32_e32 v145, v37
	v_mov_b32_e32 v144, v37
	v_mov_b32_e32 v143, v37
	v_mov_b32_e32 v142, v37
	v_mov_b32_e32 v141, v37
	v_mov_b32_e32 v140, v37
	v_mov_b32_e32 v139, v37
	v_mov_b32_e32 v138, v37
	v_mov_b32_e32 v129, v37
	v_mov_b32_e32 v128, v37
	v_mov_b32_e32 v127, v37
	v_mov_b32_e32 v126, v37
	v_mov_b32_e32 v125, v37
	v_mov_b32_e32 v124, v37
	v_mov_b32_e32 v123, v37
	v_mov_b32_e32 v122, v37
	v_mov_b32_e32 v113, v37
	v_mov_b32_e32 v112, v37
	v_mov_b32_e32 v111, v37
	v_mov_b32_e32 v110, v37
	v_mov_b32_e32 v109, v37
	v_mov_b32_e32 v108, v37
	v_mov_b32_e32 v107, v37
	v_mov_b32_e32 v106, v37
	v_mov_b32_e32 v153, v37
	v_mov_b32_e32 v152, v37
	v_mov_b32_e32 v151, v37
	v_mov_b32_e32 v150, v37
	v_mov_b32_e32 v149, v37
	v_mov_b32_e32 v148, v37
	v_mov_b32_e32 v147, v37
	v_mov_b32_e32 v146, v37
	v_mov_b32_e32 v137, v37
	v_mov_b32_e32 v136, v37
	v_mov_b32_e32 v135, v37
	v_mov_b32_e32 v134, v37
	v_mov_b32_e32 v133, v37
	v_mov_b32_e32 v132, v37
	v_mov_b32_e32 v131, v37
	v_mov_b32_e32 v130, v37
	v_mov_b32_e32 v121, v37
	v_mov_b32_e32 v120, v37
	v_mov_b32_e32 v119, v37
	v_mov_b32_e32 v118, v37
	v_mov_b32_e32 v117, v37
	v_mov_b32_e32 v116, v37
	v_mov_b32_e32 v115, v37
	v_mov_b32_e32 v114, v37
	v_mov_b32_e32 v105, v37
	v_mov_b32_e32 v104, v37
	v_mov_b32_e32 v103, v37
	v_mov_b32_e32 v102, v37
	v_mov_b32_e32 v101, v37
	v_mov_b32_e32 v100, v37
	v_mov_b32_e32 v99, v37
	v_mov_b32_e32 v98, v37
	v_mov_b32_e32 v97, v37
	v_mov_b32_e32 v96, v37
	v_mov_b32_e32 v95, v37
	v_mov_b32_e32 v94, v37
	v_mov_b32_e32 v93, v37
	v_mov_b32_e32 v92, v37
	v_mov_b32_e32 v91, v37
	v_mov_b32_e32 v90, v37
	v_mov_b32_e32 v81, v37
	v_mov_b32_e32 v80, v37
	v_mov_b32_e32 v79, v37
	v_mov_b32_e32 v78, v37
	v_mov_b32_e32 v77, v37
	v_mov_b32_e32 v76, v37
	v_mov_b32_e32 v75, v37
	v_mov_b32_e32 v74, v37
	v_mov_b32_e32 v65, v37
	v_mov_b32_e32 v64, v37
	v_mov_b32_e32 v63, v37
	v_mov_b32_e32 v62, v37
	v_mov_b32_e32 v61, v37
	v_mov_b32_e32 v60, v37
	v_mov_b32_e32 v59, v37
	v_mov_b32_e32 v58, v37
	v_mov_b32_e32 v49, v37
	v_mov_b32_e32 v48, v37
	v_mov_b32_e32 v47, v37
	v_mov_b32_e32 v46, v37
	v_mov_b32_e32 v45, v37
	v_mov_b32_e32 v44, v37
	v_mov_b32_e32 v43, v37
	v_mov_b32_e32 v42, v37
	s_branch .LBB0_205
.Lzk_1:
	s_add_u32 s2, s50, 0x80
	s_addc_u32 s3, s51, 0
	s_add_u32 s20, s48, 0x100
	v_mov_b32_e32 v42, 0
	s_addc_u32 s52, s49, 0
	s_mov_b32 s48, 0
	v_mov_b32_e32 v43, v42
	v_mov_b32_e32 v44, v42
	v_mov_b32_e32 v45, v42
	v_mov_b32_e32 v46, v42
	v_mov_b32_e32 v47, v42
	v_mov_b32_e32 v48, v42
	v_mov_b32_e32 v49, v42
	v_mov_b32_e32 v58, v42
	v_mov_b32_e32 v59, v42
	v_mov_b32_e32 v60, v42
	v_mov_b32_e32 v61, v42
	v_mov_b32_e32 v62, v42
	v_mov_b32_e32 v63, v42
	v_mov_b32_e32 v64, v42
	v_mov_b32_e32 v65, v42
	v_mov_b32_e32 v74, v42
	v_mov_b32_e32 v75, v42
	v_mov_b32_e32 v76, v42
	v_mov_b32_e32 v77, v42
	v_mov_b32_e32 v78, v42
	v_mov_b32_e32 v79, v42
	v_mov_b32_e32 v80, v42
	v_mov_b32_e32 v81, v42
	v_mov_b32_e32 v90, v42
	v_mov_b32_e32 v91, v42
	v_mov_b32_e32 v92, v42
	v_mov_b32_e32 v93, v42
	v_mov_b32_e32 v94, v42
	v_mov_b32_e32 v95, v42
	v_mov_b32_e32 v96, v42
	v_mov_b32_e32 v97, v42
	v_mov_b32_e32 v98, v42
	v_mov_b32_e32 v99, v42
	v_mov_b32_e32 v100, v42
	v_mov_b32_e32 v101, v42
	v_mov_b32_e32 v102, v42
	v_mov_b32_e32 v103, v42
	v_mov_b32_e32 v104, v42
	v_mov_b32_e32 v105, v42
	v_mov_b32_e32 v114, v42
	v_mov_b32_e32 v115, v42
	v_mov_b32_e32 v116, v42
	v_mov_b32_e32 v117, v42
	v_mov_b32_e32 v118, v42
	v_mov_b32_e32 v119, v42
	v_mov_b32_e32 v120, v42
	v_mov_b32_e32 v121, v42
	v_mov_b32_e32 v130, v42
	v_mov_b32_e32 v131, v42
	v_mov_b32_e32 v132, v42
	v_mov_b32_e32 v133, v42
	v_mov_b32_e32 v134, v42
	v_mov_b32_e32 v135, v42
	v_mov_b32_e32 v136, v42
	v_mov_b32_e32 v137, v42
	v_mov_b32_e32 v146, v42
	v_mov_b32_e32 v147, v42
	v_mov_b32_e32 v148, v42
	v_mov_b32_e32 v149, v42
	v_mov_b32_e32 v150, v42
	v_mov_b32_e32 v151, v42
	v_mov_b32_e32 v152, v42
	v_mov_b32_e32 v153, v42
	v_mov_b32_e32 v106, v42
	v_mov_b32_e32 v107, v42
	v_mov_b32_e32 v108, v42
	v_mov_b32_e32 v109, v42
	v_mov_b32_e32 v110, v42
	v_mov_b32_e32 v111, v42
	v_mov_b32_e32 v112, v42
	v_mov_b32_e32 v113, v42
	v_mov_b32_e32 v122, v42
	v_mov_b32_e32 v123, v42
	v_mov_b32_e32 v124, v42
	v_mov_b32_e32 v125, v42
	v_mov_b32_e32 v126, v42
	v_mov_b32_e32 v127, v42
	v_mov_b32_e32 v128, v42
	v_mov_b32_e32 v129, v42
	v_mov_b32_e32 v138, v42
	v_mov_b32_e32 v139, v42
	v_mov_b32_e32 v140, v42
	v_mov_b32_e32 v141, v42
	v_mov_b32_e32 v142, v42
	v_mov_b32_e32 v143, v42
	v_mov_b32_e32 v144, v42
	v_mov_b32_e32 v145, v42
	v_mov_b32_e32 v154, v42
	v_mov_b32_e32 v155, v42
	v_mov_b32_e32 v156, v42
	v_mov_b32_e32 v157, v42
	v_mov_b32_e32 v158, v42
	v_mov_b32_e32 v159, v42
	v_mov_b32_e32 v160, v42
	v_mov_b32_e32 v161, v42
	v_mov_b32_e32 v86, v42
	v_mov_b32_e32 v87, v42
	v_mov_b32_e32 v88, v42
	v_mov_b32_e32 v89, v42
	v_mov_b32_e32 v82, v42
	v_mov_b32_e32 v83, v42
	v_mov_b32_e32 v84, v42
	v_mov_b32_e32 v85, v42
	v_mov_b32_e32 v70, v42
	v_mov_b32_e32 v71, v42
	v_mov_b32_e32 v72, v42
	v_mov_b32_e32 v73, v42
	v_mov_b32_e32 v66, v42
	v_mov_b32_e32 v67, v42
	v_mov_b32_e32 v68, v42
	v_mov_b32_e32 v69, v42
	v_mov_b32_e32 v54, v42
	v_mov_b32_e32 v55, v42
	v_mov_b32_e32 v56, v42
	v_mov_b32_e32 v57, v42
	v_mov_b32_e32 v50, v42
	v_mov_b32_e32 v51, v42
	v_mov_b32_e32 v52, v42
	v_mov_b32_e32 v53, v42
	v_mov_b32_e32 v38, v42
	v_mov_b32_e32 v39, v42
	v_mov_b32_e32 v40, v42
	v_mov_b32_e32 v41, v42
	v_mov_b32_e32 v34, v42
	v_mov_b32_e32 v35, v42
	v_mov_b32_e32 v36, v42
	v_mov_b32_e32 v37, v42

; template <class Epi, class Sched, bool ALIGN_EPI = false, bool SP2 = false>
; __device__ __forceinline__ void gemm_phase(PG8_LAS unsigned char* lds, const Gemm g, const Sched& S, const Epi& E) {
;     ...
;         for (int a = 0; a < 2; ++a)
; #pragma unroll
;             for (int b = 0; b < 2; ++b)
; #pragma unroll
;                 for (int m = 0; m < 4; ++m)
; #pragma unroll
;                     for (int n = 0; n < 2; ++n) acc[a][b][m][n] = (f32x4){0.f, 0.f, 0.f, 0.f};
;         cur = nxt; cA = nA; cB = nB; ++ui;
.LBB0_980:
	v_mov_b32_e32 v5, 0
	s_andn2_b64 vcc, exec, s[28:29]
	s_cbranch_vccz .Lzk_2
	v_mov_b32_e32 v4, v5
	v_mov_b32_e32 v3, v5
	v_mov_b32_e32 v2, v5
	v_mov_b32_e32 v9, v5
	v_mov_b32_e32 v8, v5
	v_mov_b32_e32 v7, v5
	v_mov_b32_e32 v6, v5
	v_mov_b32_e32 v21, v5
	v_mov_b32_e32 v20, v5
	v_mov_b32_e32 v19, v5
	v_mov_b32_e32 v18, v5
	v_mov_b32_e32 v25, v5
	v_mov_b32_e32 v24, v5
	v_mov_b32_e32 v23, v5
	v_mov_b32_e32 v22, v5
	v_mov_b32_e32 v37, v5
	v_mov_b32_e32 v36, v5
	v_mov_b32_e32 v35, v5
	v_mov_b32_e32 v34, v5
	v_mov_b32_e32 v41, v5
	v_mov_b32_e32 v40, v5
	v_mov_b32_e32 v39, v5
	v_mov_b32_e32 v38, v5
	v_mov_b32_e32 v53, v5
	v_mov_b32_e32 v52, v5
	v_mov_b32_e32 v51, v5
	v_mov_b32_e32 v50, v5
	v_mov_b32_e32 v57, v5
	v_mov_b32_e32 v56, v5
	v_mov_b32_e32 v55, v5
	v_mov_b32_e32 v54, v5
	v_mov_b32_e32 v129, v5
	v_mov_b32_e32 v128, v5
	v_mov_b32_e32 v127, v5
	v_mov_b32_e32 v126, v5
	v_mov_b32_e32 v125, v5
	v_mov_b32_e32 v124, v5
	v_mov_b32_e32 v123, v5
	v_mov_b32_e32 v122, v5
	v_mov_b32_e32 v113, v5
	v_mov_b32_e32 v112, v5
	v_mov_b32_e32 v111, v5
	v_mov_b32_e32 v110, v5
	v_mov_b32_e32 v109, v5
	v_mov_b32_e32 v108, v5
	v_mov_b32_e32 v107, v5
	v_mov_b32_e32 v106, v5
	v_mov_b32_e32 v97, v5
	v_mov_b32_e32 v96, v5
	v_mov_b32_e32 v95, v5
	v_mov_b32_e32 v94, v5
	v_mov_b32_e32 v93, v5
	v_mov_b32_e32 v92, v5
	v_mov_b32_e32 v91, v5
	v_mov_b32_e32 v90, v5
	v_mov_b32_e32 v81, v5
	v_mov_b32_e32 v80, v5
	v_mov_b32_e32 v79, v5
	v_mov_b32_e32 v78, v5
	v_mov_b32_e32 v77, v5
	v_mov_b32_e32 v76, v5
	v_mov_b32_e32 v75, v5
	v_mov_b32_e32 v74, v5
	v_mov_b32_e32 v121, v5
	v_mov_b32_e32 v120, v5
	v_mov_b32_e32 v119, v5
	v_mov_b32_e32 v118, v5
	v_mov_b32_e32 v117, v5
	v_mov_b32_e32 v116, v5
	v_mov_b32_e32 v115, v5
	v_mov_b32_e32 v114, v5
	v_mov_b32_e32 v105, v5
	v_mov_b32_e32 v104, v5
	v_mov_b32_e32 v103, v5
	v_mov_b32_e32 v102, v5
	v_mov_b32_e32 v101, v5
	v_mov_b32_e32 v100, v5
	v_mov_b32_e32 v99, v5
	v_mov_b32_e32 v98, v5
	v_mov_b32_e32 v89, v5
	v_mov_b32_e32 v88, v5
	v_mov_b32_e32 v87, v5
	v_mov_b32_e32 v86, v5
	v_mov_b32_e32 v85, v5
	v_mov_b32_e32 v84, v5
	v_mov_b32_e32 v83, v5
	v_mov_b32_e32 v82, v5
	v_mov_b32_e32 v73, v5
	v_mov_b32_e32 v72, v5
	v_mov_b32_e32 v71, v5
	v_mov_b32_e32 v70, v5
	v_mov_b32_e32 v69, v5
	v_mov_b32_e32 v68, v5
	v_mov_b32_e32 v67, v5
	v_mov_b32_e32 v66, v5
	v_mov_b32_e32 v65, v5
	v_mov_b32_e32 v64, v5
	v_mov_b32_e32 v63, v5
	v_mov_b32_e32 v62, v5
	v_mov_b32_e32 v61, v5
	v_mov_b32_e32 v60, v5
	v_mov_b32_e32 v59, v5
	v_mov_b32_e32 v58, v5
	v_mov_b32_e32 v49, v5
	v_mov_b32_e32 v48, v5
	v_mov_b32_e32 v47, v5
	v_mov_b32_e32 v46, v5
	v_mov_b32_e32 v45, v5
	v_mov_b32_e32 v44, v5
	v_mov_b32_e32 v43, v5
	v_mov_b32_e32 v42, v5
	v_mov_b32_e32 v33, v5
	v_mov_b32_e32 v32, v5
	v_mov_b32_e32 v31, v5
	v_mov_b32_e32 v30, v5
	v_mov_b32_e32 v29, v5
	v_mov_b32_e32 v28, v5
	v_mov_b32_e32 v27, v5
	v_mov_b32_e32 v26, v5
	v_mov_b32_e32 v17, v5
	v_mov_b32_e32 v16, v5
	v_mov_b32_e32 v15, v5
	v_mov_b32_e32 v14, v5
	v_mov_b32_e32 v13, v5
	v_mov_b32_e32 v12, v5
	v_mov_b32_e32 v11, v5
	v_mov_b32_e32 v10, v5
	s_branch .LBB0_985
;     __device__ __forceinline__ void mid(f32x4 (&acc)[2][2][4][2], const Unit& u, int wr, int wc, int fr, int fq) const {
;     ...
;                     for (int bj = 0; bj < 2; ++bj) { const size_t o = (size_t)(u.pm * BM + wr * 64 + fr + ai * HALF + (2 * mp + mm) * 16) * 2048 + u.pn * BM + wc * 64 + bj * 32 + 8 * fq;
;                         ga[mm][bj] = *(const uint2*)(gate + o); gm[mm][bj] = *(const uint2*)(gate + o + 1024); }
; template <class Epi, class Sched, bool ALIGN_EPI = false, bool SP2 = false>
; __device__ __forceinline__ void gemm_phase(PG8_LAS unsigned char* lds, const Gemm g, const Sched& S, const Epi& E) {
;     ...
;         for (int a = 0; a < 2; ++a)
; #pragma unroll
;             for (int b = 0; b < 2; ++b)
; #pragma unroll
;                 for (int m = 0; m < 4; ++m)
; #pragma unroll
;                     for (int n = 0; n < 2; ++n) acc[a][b][m][n] = (f32x4){0.f, 0.f, 0.f, 0.f};
;         cur = nxt; cA = nA; cB = nB; ++ui;
.Lzk_2:
	s_lshl_b32 s33, s69, 8
	v_add_u32_e32 v2, s33, v172
	v_ashrrev_i32_e32 v3, 31, v2
	s_lshl_b32 s0, s71, 8
	v_lshlrev_b64 v[6:7], 11, v[2:3]
	v_or_b32_e32 v2, 16, v2
	s_ashr_i32 s1, s0, 31
	v_ashrrev_i32_e32 v3, 31, v2
	v_lshl_add_u64 v[4:5], v[142:143], 0, s[0:1]
	v_lshlrev_b64 v[2:3], 11, v[2:3]
	v_lshl_add_u64 v[150:151], v[4:5], 0, v[2:3]
	v_or_b32_e32 v2, 32, v172
	v_add_u32_e32 v2, s33, v2
	v_ashrrev_i32_e32 v3, 31, v2
	v_lshl_add_u64 v[148:149], v[4:5], 0, v[6:7]
	v_lshlrev_b64 v[6:7], 11, v[2:3]
	v_or_b32_e32 v2, 16, v2
	v_ashrrev_i32_e32 v3, 31, v2
	v_lshlrev_b64 v[2:3], 11, v[2:3]
	v_lshl_add_u64 v[154:155], v[4:5], 0, v[2:3]
	v_add_u32_e32 v2, 0x80, v172
	v_add_u32_e32 v2, s33, v2
	v_ashrrev_i32_e32 v3, 31, v2
	v_lshl_add_u64 v[152:153], v[4:5], 0, v[6:7]
	v_lshlrev_b64 v[6:7], 11, v[2:3]
	v_or_b32_e32 v2, 16, v2
	v_ashrrev_i32_e32 v3, 31, v2
	v_lshlrev_b64 v[2:3], 11, v[2:3]
	v_lshl_add_u64 v[158:159], v[4:5], 0, v[2:3]
	v_add_u32_e32 v2, 0xa0, v172
	v_add_u32_e32 v2, s33, v2
	v_ashrrev_i32_e32 v3, 31, v2
	v_lshl_add_u64 v[156:157], v[4:5], 0, v[6:7]
	v_lshlrev_b64 v[6:7], 11, v[2:3]
	v_or_b32_e32 v2, 16, v2
	v_ashrrev_i32_e32 v3, 31, v2
	v_lshlrev_b64 v[2:3], 11, v[2:3]
	s_add_u32 s73, s40, 0x100
	v_mov_b32_e32 v10, 0
	v_lshl_add_u64 v[160:161], v[4:5], 0, v[6:7]
	v_lshl_add_u64 v[162:163], v[4:5], 0, v[2:3]
	s_addc_u32 s74, s41, 0
	v_lshl_add_u64 v[164:165], s[38:39], 0, v[144:145]
	v_lshl_add_u64 v[166:167], s[38:39], 0, v[146:147]
	s_mov_b32 s42, 0
	s_mov_b64 s[40:41], 0
	v_mov_b32_e32 v11, v10
	v_mov_b32_e32 v12, v10
	v_mov_b32_e32 v13, v10
	v_mov_b32_e32 v14, v10
	v_mov_b32_e32 v15, v10
	v_mov_b32_e32 v16, v10
	v_mov_b32_e32 v17, v10
	v_mov_b32_e32 v26, v10
	v_mov_b32_e32 v27, v10
	v_mov_b32_e32 v28, v10
	v_mov_b32_e32 v29, v10
	v_mov_b32_e32 v30, v10
	v_mov_b32_e32 v31, v10
	v_mov_b32_e32 v32, v10
	v_mov_b32_e32 v33, v10
	v_mov_b32_e32 v42, v10
	v_mov_b32_e32 v43, v10
	v_mov_b32_e32 v44, v10
	v_mov_b32_e32 v45, v10
	v_mov_b32_e32 v46, v10
	v_mov_b32_e32 v47, v10
	v_mov_b32_e32 v48, v10
	v_mov_b32_e32 v49, v10
	v_mov_b32_e32 v58, v10
	v_mov_b32_e32 v59, v10
	v_mov_b32_e32 v60, v10
	v_mov_b32_e32 v61, v10
	v_mov_b32_e32 v62, v10
	v_mov_b32_e32 v63, v10
	v_mov_b32_e32 v64, v10
	v_mov_b32_e32 v65, v10
	v_mov_b32_e32 v66, v10
	v_mov_b32_e32 v67, v10
	v_mov_b32_e32 v68, v10
	v_mov_b32_e32 v69, v10
	v_mov_b32_e32 v70, v10
	v_mov_b32_e32 v71, v10
	v_mov_b32_e32 v72, v10
	v_mov_b32_e32 v73, v10
	v_mov_b32_e32 v82, v10
	v_mov_b32_e32 v83, v10
	v_mov_b32_e32 v84, v10
	v_mov_b32_e32 v85, v10
	v_mov_b32_e32 v86, v10
	v_mov_b32_e32 v87, v10
	v_mov_b32_e32 v88, v10
	v_mov_b32_e32 v89, v10
	v_mov_b32_e32 v98, v10
	v_mov_b32_e32 v99, v10
	v_mov_b32_e32 v100, v10
	v_mov_b32_e32 v101, v10
	v_mov_b32_e32 v102, v10
	v_mov_b32_e32 v103, v10
	v_mov_b32_e32 v104, v10
	v_mov_b32_e32 v105, v10
	v_mov_b32_e32 v114, v10
	v_mov_b32_e32 v115, v10
	v_mov_b32_e32 v116, v10
	v_mov_b32_e32 v117, v10
	v_mov_b32_e32 v118, v10
	v_mov_b32_e32 v119, v10
	v_mov_b32_e32 v120, v10
	v_mov_b32_e32 v121, v10
	v_mov_b32_e32 v74, v10
	v_mov_b32_e32 v75, v10
	v_mov_b32_e32 v76, v10
	v_mov_b32_e32 v77, v10
	v_mov_b32_e32 v78, v10
	v_mov_b32_e32 v79, v10
	v_mov_b32_e32 v80, v10
	v_mov_b32_e32 v81, v10
	v_mov_b32_e32 v90, v10
	v_mov_b32_e32 v91, v10
	v_mov_b32_e32 v92, v10
	v_mov_b32_e32 v93, v10
	v_mov_b32_e32 v94, v10
	v_mov_b32_e32 v95, v10
	v_mov_b32_e32 v96, v10
	v_mov_b32_e32 v97, v10
	v_mov_b32_e32 v106, v10
	v_mov_b32_e32 v107, v10
	v_mov_b32_e32 v108, v10
	v_mov_b32_e32 v109, v10
	v_mov_b32_e32 v110, v10
	v_mov_b32_e32 v111, v10
	v_mov_b32_e32 v112, v10
	v_mov_b32_e32 v113, v10
	v_mov_b32_e32 v122, v10
	v_mov_b32_e32 v123, v10
	v_mov_b32_e32 v124, v10
	v_mov_b32_e32 v125, v10
	v_mov_b32_e32 v126, v10
	v_mov_b32_e32 v127, v10
	v_mov_b32_e32 v128, v10
	v_mov_b32_e32 v129, v10
	v_mov_b32_e32 v54, v10
	v_mov_b32_e32 v55, v10
	v_mov_b32_e32 v56, v10
	v_mov_b32_e32 v57, v10
	v_mov_b32_e32 v50, v10
	v_mov_b32_e32 v51, v10
	v_mov_b32_e32 v52, v10
	v_mov_b32_e32 v53, v10
	v_mov_b32_e32 v38, v10
	v_mov_b32_e32 v39, v10
	v_mov_b32_e32 v40, v10
	v_mov_b32_e32 v41, v10
	v_mov_b32_e32 v34, v10
	v_mov_b32_e32 v35, v10
	v_mov_b32_e32 v36, v10
	v_mov_b32_e32 v37, v10
	v_mov_b32_e32 v22, v10
	v_mov_b32_e32 v23, v10
	v_mov_b32_e32 v24, v10
	v_mov_b32_e32 v25, v10
	v_mov_b32_e32 v18, v10
	v_mov_b32_e32 v19, v10
	v_mov_b32_e32 v20, v10
	v_mov_b32_e32 v21, v10
	v_mov_b32_e32 v6, v10
	v_mov_b32_e32 v7, v10
	v_mov_b32_e32 v8, v10
	v_mov_b32_e32 v9, v10
	v_mov_b32_e32 v2, v10
	v_mov_b32_e32 v3, v10
	v_mov_b32_e32 v4, v10
	v_mov_b32_e32 v5, v10
	s_cmp_lg_u32 s56, s42
	s_cbranch_scc1 .LBB0_984
	s_branch .LBB0_983

; template <class Epi, class Sched, bool ALIGN_EPI = false, bool SP2 = false>
; __device__ __forceinline__ void gemm_phase(PG8_LAS unsigned char* lds, const Gemm g, const Sched& S, const Epi& E) {
;     ...
;         for (int t = 0; t < nt; t += 2) {
;             if constexpr (Epi::MIDK) { if (t == (nt >> 1)) E.mid(acc, cur, wr, wc, fr, fq); }
;             const bool last = (t == nt - 2);
;             const char* a1 = cA + (size_t)(t + 1) * kstep;
;             const char* a2 = last ? nA : cA + (size_t)(t + 2) * kstep; const char* b2 = last ? nB : cB + (size_t)(t + 2) * kstep;
;             const char* a3 = a2 + kstep; const char* b3 = b2 + kstep;
;     ...
;         for (int a = 0; a < 2; ++a)
; #pragma unroll
;             for (int b = 0; b < 2; ++b)
; #pragma unroll
;                 for (int m = 0; m < 4; ++m)
; #pragma unroll
;                     for (int n = 0; n < 2; ++n) acc[a][b][m][n] = (f32x4){0.f, 0.f, 0.f, 0.f};
;         cur = nxt; cA = nA; cB = nB; ++ui;
.LBB0_1068:
	v_mov_b32_e32 v5, 0
	s_andn2_b64 vcc, exec, s[30:31]
	s_waitcnt lgkmcnt(0)
	s_cbranch_vccz .Lzk_3
	v_mov_b32_e32 v4, v5
	v_mov_b32_e32 v3, v5
	v_mov_b32_e32 v2, v5
	v_mov_b32_e32 v13, v5
	v_mov_b32_e32 v12, v5
	v_mov_b32_e32 v11, v5
	v_mov_b32_e32 v10, v5
	v_mov_b32_e32 v21, v5
	v_mov_b32_e32 v20, v5
	v_mov_b32_e32 v19, v5
	v_mov_b32_e32 v18, v5
	v_mov_b32_e32 v25, v5
	v_mov_b32_e32 v24, v5
	v_mov_b32_e32 v23, v5
	v_mov_b32_e32 v22, v5
	v_mov_b32_e32 v37, v5
	v_mov_b32_e32 v36, v5
	v_mov_b32_e32 v35, v5
	v_mov_b32_e32 v34, v5
	v_mov_b32_e32 v41, v5
	v_mov_b32_e32 v40, v5
	v_mov_b32_e32 v39, v5
	v_mov_b32_e32 v38, v5
	v_mov_b32_e32 v73, v5
	v_mov_b32_e32 v72, v5
	v_mov_b32_e32 v71, v5
	v_mov_b32_e32 v70, v5
	v_mov_b32_e32 v69, v5
	v_mov_b32_e32 v68, v5
	v_mov_b32_e32 v67, v5
	v_mov_b32_e32 v66, v5
	v_mov_b32_e32 v129, v5
	v_mov_b32_e32 v128, v5
	v_mov_b32_e32 v127, v5
	v_mov_b32_e32 v126, v5
	v_mov_b32_e32 v125, v5
	v_mov_b32_e32 v124, v5
	v_mov_b32_e32 v123, v5
	v_mov_b32_e32 v122, v5
	v_mov_b32_e32 v61, v5
	v_mov_b32_e32 v60, v5
	v_mov_b32_e32 v59, v5
	v_mov_b32_e32 v58, v5
	v_mov_b32_e32 v65, v5
	v_mov_b32_e32 v64, v5
	v_mov_b32_e32 v63, v5
	v_mov_b32_e32 v62, v5
	v_mov_b32_e32 v109, v5
	v_mov_b32_e32 v108, v5
	v_mov_b32_e32 v107, v5
	v_mov_b32_e32 v106, v5
	v_mov_b32_e32 v113, v5
	v_mov_b32_e32 v112, v5
	v_mov_b32_e32 v111, v5
	v_mov_b32_e32 v110, v5
	v_mov_b32_e32 v101, v5
	v_mov_b32_e32 v100, v5
	v_mov_b32_e32 v99, v5
	v_mov_b32_e32 v98, v5
	v_mov_b32_e32 v105, v5
	v_mov_b32_e32 v104, v5
	v_mov_b32_e32 v103, v5
	v_mov_b32_e32 v102, v5
	v_mov_b32_e32 v121, v5
	v_mov_b32_e32 v120, v5
	v_mov_b32_e32 v119, v5
	v_mov_b32_e32 v118, v5
	v_mov_b32_e32 v117, v5
	v_mov_b32_e32 v116, v5
	v_mov_b32_e32 v115, v5
	v_mov_b32_e32 v114, v5
	v_mov_b32_e32 v53, v5
	v_mov_b32_e32 v52, v5
	v_mov_b32_e32 v51, v5
	v_mov_b32_e32 v50, v5
	v_mov_b32_e32 v57, v5
	v_mov_b32_e32 v56, v5
	v_mov_b32_e32 v55, v5
	v_mov_b32_e32 v54, v5
	v_mov_b32_e32 v93, v5
	v_mov_b32_e32 v92, v5
	v_mov_b32_e32 v91, v5
	v_mov_b32_e32 v90, v5
	v_mov_b32_e32 v97, v5
	v_mov_b32_e32 v96, v5
	v_mov_b32_e32 v95, v5
	v_mov_b32_e32 v94, v5
	v_mov_b32_e32 v77, v5
	v_mov_b32_e32 v76, v5
	v_mov_b32_e32 v75, v5
	v_mov_b32_e32 v74, v5
	v_mov_b32_e32 v81, v5
	v_mov_b32_e32 v80, v5
	v_mov_b32_e32 v79, v5
	v_mov_b32_e32 v78, v5
	v_mov_b32_e32 v85, v5
	v_mov_b32_e32 v84, v5
	v_mov_b32_e32 v83, v5
	v_mov_b32_e32 v82, v5
	v_mov_b32_e32 v89, v5
	v_mov_b32_e32 v88, v5
	v_mov_b32_e32 v87, v5
	v_mov_b32_e32 v86, v5
	v_mov_b32_e32 v49, v5
	v_mov_b32_e32 v48, v5
	v_mov_b32_e32 v47, v5
	v_mov_b32_e32 v46, v5
	v_mov_b32_e32 v45, v5
	v_mov_b32_e32 v44, v5
	v_mov_b32_e32 v43, v5
	v_mov_b32_e32 v42, v5
	v_mov_b32_e32 v33, v5
	v_mov_b32_e32 v32, v5
	v_mov_b32_e32 v31, v5
	v_mov_b32_e32 v30, v5
	v_mov_b32_e32 v29, v5
	v_mov_b32_e32 v28, v5
	v_mov_b32_e32 v27, v5
	v_mov_b32_e32 v26, v5
	v_mov_b32_e32 v17, v5
	v_mov_b32_e32 v16, v5
	v_mov_b32_e32 v15, v5
	v_mov_b32_e32 v14, v5
	v_mov_b32_e32 v9, v5
	v_mov_b32_e32 v8, v5
	v_mov_b32_e32 v7, v5
	v_mov_b32_e32 v6, v5
	s_branch .LBB0_1072
.Lzk_3:
	s_add_u32 s56, s56, 0x80
	s_addc_u32 s57, s57, 0
	s_add_u32 s93, s58, 0x100
	v_mov_b32_e32 v6, 0
	s_addc_u32 s94, s59, 0
	s_mov_b32 s58, 0
	v_mov_b32_e32 v7, v6
	v_mov_b32_e32 v8, v6
	v_mov_b32_e32 v9, v6
	v_mov_b32_e32 v14, v6
	v_mov_b32_e32 v15, v6
	v_mov_b32_e32 v16, v6
	v_mov_b32_e32 v17, v6
	v_mov_b32_e32 v26, v6
	v_mov_b32_e32 v27, v6
	v_mov_b32_e32 v28, v6
	v_mov_b32_e32 v29, v6
	v_mov_b32_e32 v30, v6
	v_mov_b32_e32 v31, v6
	v_mov_b32_e32 v32, v6
	v_mov_b32_e32 v33, v6
	v_mov_b32_e32 v42, v6
	v_mov_b32_e32 v43, v6
	v_mov_b32_e32 v44, v6
	v_mov_b32_e32 v45, v6
	v_mov_b32_e32 v46, v6
	v_mov_b32_e32 v47, v6
	v_mov_b32_e32 v48, v6
	v_mov_b32_e32 v49, v6
	v_mov_b32_e32 v86, v6
	v_mov_b32_e32 v87, v6
	v_mov_b32_e32 v88, v6
	v_mov_b32_e32 v89, v6
	v_mov_b32_e32 v82, v6
	v_mov_b32_e32 v83, v6
	v_mov_b32_e32 v84, v6
	v_mov_b32_e32 v85, v6
	v_mov_b32_e32 v78, v6
	v_mov_b32_e32 v79, v6
	v_mov_b32_e32 v80, v6
	v_mov_b32_e32 v81, v6
	v_mov_b32_e32 v74, v6
	v_mov_b32_e32 v75, v6
	v_mov_b32_e32 v76, v6
	v_mov_b32_e32 v77, v6
	v_mov_b32_e32 v94, v6
	v_mov_b32_e32 v95, v6
	v_mov_b32_e32 v96, v6
	v_mov_b32_e32 v97, v6
	v_mov_b32_e32 v90, v6
	v_mov_b32_e32 v91, v6
	v_mov_b32_e32 v92, v6
	v_mov_b32_e32 v93, v6
	v_mov_b32_e32 v54, v6
	v_mov_b32_e32 v55, v6
	v_mov_b32_e32 v56, v6
	v_mov_b32_e32 v57, v6
	v_mov_b32_e32 v50, v6
	v_mov_b32_e32 v51, v6
	v_mov_b32_e32 v52, v6
	v_mov_b32_e32 v53, v6
	v_mov_b32_e32 v114, v6
	v_mov_b32_e32 v115, v6
	v_mov_b32_e32 v116, v6
	v_mov_b32_e32 v117, v6
	v_mov_b32_e32 v118, v6
	v_mov_b32_e32 v119, v6
	v_mov_b32_e32 v120, v6
	v_mov_b32_e32 v121, v6
	v_mov_b32_e32 v102, v6
	v_mov_b32_e32 v103, v6
	v_mov_b32_e32 v104, v6
	v_mov_b32_e32 v105, v6
	v_mov_b32_e32 v98, v6
	v_mov_b32_e32 v99, v6
	v_mov_b32_e32 v100, v6
	v_mov_b32_e32 v101, v6
	v_mov_b32_e32 v110, v6
	v_mov_b32_e32 v111, v6
	v_mov_b32_e32 v112, v6
	v_mov_b32_e32 v113, v6
	v_mov_b32_e32 v106, v6
	v_mov_b32_e32 v107, v6
	v_mov_b32_e32 v108, v6
	v_mov_b32_e32 v109, v6
	v_mov_b32_e32 v62, v6
	v_mov_b32_e32 v63, v6
	v_mov_b32_e32 v64, v6
	v_mov_b32_e32 v65, v6
	v_mov_b32_e32 v58, v6
	v_mov_b32_e32 v59, v6
	v_mov_b32_e32 v60, v6
	v_mov_b32_e32 v61, v6
	v_mov_b32_e32 v122, v6
	v_mov_b32_e32 v123, v6
	v_mov_b32_e32 v124, v6
	v_mov_b32_e32 v125, v6
	v_mov_b32_e32 v126, v6
	v_mov_b32_e32 v127, v6
	v_mov_b32_e32 v128, v6
	v_mov_b32_e32 v129, v6
	v_mov_b32_e32 v66, v6
	v_mov_b32_e32 v67, v6
	v_mov_b32_e32 v68, v6
	v_mov_b32_e32 v69, v6
	v_mov_b32_e32 v70, v6
	v_mov_b32_e32 v71, v6
	v_mov_b32_e32 v72, v6
	v_mov_b32_e32 v73, v6
	v_mov_b32_e32 v38, v6
	v_mov_b32_e32 v39, v6
	v_mov_b32_e32 v40, v6
	v_mov_b32_e32 v41, v6
	v_mov_b32_e32 v34, v6
	v_mov_b32_e32 v35, v6
	v_mov_b32_e32 v36, v6
	v_mov_b32_e32 v37, v6
	v_mov_b32_e32 v22, v6
	v_mov_b32_e32 v23, v6
	v_mov_b32_e32 v24, v6
	v_mov_b32_e32 v25, v6
	v_mov_b32_e32 v18, v6
	v_mov_b32_e32 v19, v6
	v_mov_b32_e32 v20, v6
	v_mov_b32_e32 v21, v6
	v_mov_b32_e32 v10, v6
	v_mov_b32_e32 v11, v6
	v_mov_b32_e32 v12, v6
	v_mov_b32_e32 v13, v6
	v_mov_b32_e32 v2, v6
	v_mov_b32_e32 v3, v6
	v_mov_b32_e32 v4, v6
	v_mov_b32_e32 v5, v6

; template <class Epi, class Sched, bool ALIGN_EPI = false, bool SP2 = false>
; __device__ __forceinline__ void gemm_phase(PG8_LAS unsigned char* lds, const Gemm g, const Sched& S, const Epi& E) {
;     ...
;         for (int t = 0; t < nt; t += 2) {
;             if constexpr (Epi::MIDK) { if (t == (nt >> 1)) E.mid(acc, cur, wr, wc, fr, fq); }
;             const bool last = (t == nt - 2);
;             const char* a1 = cA + (size_t)(t + 1) * kstep;
;             const char* a2 = last ? nA : cA + (size_t)(t + 2) * kstep; const char* b2 = last ? nB : cB + (size_t)(t + 2) * kstep;
;             const char* a3 = a2 + kstep; const char* b3 = b2 + kstep;
;     ...
;         for (int a = 0; a < 2; ++a)
; #pragma unroll
;             for (int b = 0; b < 2; ++b)
; #pragma unroll
;                 for (int m = 0; m < 4; ++m)
; #pragma unroll
;                     for (int n = 0; n < 2; ++n) acc[a][b][m][n] = (f32x4){0.f, 0.f, 0.f, 0.f};
;         cur = nxt; cA = nA; cB = nB; ++ui;
.LBB0_1169:
	v_mov_b32_e32 v5, 0
	s_andn2_b64 vcc, exec, s[24:25]
	s_cbranch_vccz .Lzk_4
	v_mov_b32_e32 v4, v5
	v_mov_b32_e32 v3, v5
	v_mov_b32_e32 v2, v5
	v_mov_b32_e32 v13, v5
	v_mov_b32_e32 v12, v5
	v_mov_b32_e32 v11, v5
	v_mov_b32_e32 v10, v5
	v_mov_b32_e32 v21, v5
	v_mov_b32_e32 v20, v5
	v_mov_b32_e32 v19, v5
	v_mov_b32_e32 v18, v5
	v_mov_b32_e32 v25, v5
	v_mov_b32_e32 v24, v5
	v_mov_b32_e32 v23, v5
	v_mov_b32_e32 v22, v5
	v_mov_b32_e32 v37, v5
	v_mov_b32_e32 v36, v5
	v_mov_b32_e32 v35, v5
	v_mov_b32_e32 v34, v5
	v_mov_b32_e32 v41, v5
	v_mov_b32_e32 v40, v5
	v_mov_b32_e32 v39, v5
	v_mov_b32_e32 v38, v5
	v_mov_b32_e32 v53, v5
	v_mov_b32_e32 v52, v5
	v_mov_b32_e32 v51, v5
	v_mov_b32_e32 v50, v5
	v_mov_b32_e32 v57, v5
	v_mov_b32_e32 v56, v5
	v_mov_b32_e32 v55, v5
	v_mov_b32_e32 v54, v5
	v_mov_b32_e32 v129, v5
	v_mov_b32_e32 v128, v5
	v_mov_b32_e32 v127, v5
	v_mov_b32_e32 v126, v5
	v_mov_b32_e32 v125, v5
	v_mov_b32_e32 v124, v5
	v_mov_b32_e32 v123, v5
	v_mov_b32_e32 v122, v5
	v_mov_b32_e32 v113, v5
	v_mov_b32_e32 v112, v5
	v_mov_b32_e32 v111, v5
	v_mov_b32_e32 v110, v5
	v_mov_b32_e32 v109, v5
	v_mov_b32_e32 v108, v5
	v_mov_b32_e32 v107, v5
	v_mov_b32_e32 v106, v5
	v_mov_b32_e32 v97, v5
	v_mov_b32_e32 v96, v5
	v_mov_b32_e32 v95, v5
	v_mov_b32_e32 v94, v5
	v_mov_b32_e32 v93, v5
	v_mov_b32_e32 v92, v5
	v_mov_b32_e32 v91, v5
	v_mov_b32_e32 v90, v5
	v_mov_b32_e32 v81, v5
	v_mov_b32_e32 v80, v5
	v_mov_b32_e32 v79, v5
	v_mov_b32_e32 v78, v5
	v_mov_b32_e32 v77, v5
	v_mov_b32_e32 v76, v5
	v_mov_b32_e32 v75, v5
	v_mov_b32_e32 v74, v5
	v_mov_b32_e32 v121, v5
	v_mov_b32_e32 v120, v5
	v_mov_b32_e32 v119, v5
	v_mov_b32_e32 v118, v5
	v_mov_b32_e32 v117, v5
	v_mov_b32_e32 v116, v5
	v_mov_b32_e32 v115, v5
	v_mov_b32_e32 v114, v5
	v_mov_b32_e32 v105, v5
	v_mov_b32_e32 v104, v5
	v_mov_b32_e32 v103, v5
	v_mov_b32_e32 v102, v5
	v_mov_b32_e32 v101, v5
	v_mov_b32_e32 v100, v5
	v_mov_b32_e32 v99, v5
	v_mov_b32_e32 v98, v5
	v_mov_b32_e32 v89, v5
	v_mov_b32_e32 v88, v5
	v_mov_b32_e32 v87, v5
	v_mov_b32_e32 v86, v5
	v_mov_b32_e32 v85, v5
	v_mov_b32_e32 v84, v5
	v_mov_b32_e32 v83, v5
	v_mov_b32_e32 v82, v5
	v_mov_b32_e32 v73, v5
	v_mov_b32_e32 v72, v5
	v_mov_b32_e32 v71, v5
	v_mov_b32_e32 v70, v5
	v_mov_b32_e32 v69, v5
	v_mov_b32_e32 v68, v5
	v_mov_b32_e32 v67, v5
	v_mov_b32_e32 v66, v5
	v_mov_b32_e32 v65, v5
	v_mov_b32_e32 v64, v5
	v_mov_b32_e32 v63, v5
	v_mov_b32_e32 v62, v5
	v_mov_b32_e32 v61, v5
	v_mov_b32_e32 v60, v5
	v_mov_b32_e32 v59, v5
	v_mov_b32_e32 v58, v5
	v_mov_b32_e32 v49, v5
	v_mov_b32_e32 v48, v5
	v_mov_b32_e32 v47, v5
	v_mov_b32_e32 v46, v5
	v_mov_b32_e32 v45, v5
	v_mov_b32_e32 v44, v5
	v_mov_b32_e32 v43, v5
	v_mov_b32_e32 v42, v5
	v_mov_b32_e32 v33, v5
	v_mov_b32_e32 v32, v5
	v_mov_b32_e32 v31, v5
	v_mov_b32_e32 v30, v5
	v_mov_b32_e32 v29, v5
	v_mov_b32_e32 v28, v5
	v_mov_b32_e32 v27, v5
	v_mov_b32_e32 v26, v5
	v_mov_b32_e32 v17, v5
	v_mov_b32_e32 v16, v5
	v_mov_b32_e32 v15, v5
	v_mov_b32_e32 v14, v5
	v_mov_b32_e32 v9, v5
	v_mov_b32_e32 v8, v5
	v_mov_b32_e32 v7, v5
	v_mov_b32_e32 v6, v5
	s_branch .LBB0_1172
.Lzk_4:
	s_add_u32 s30, s30, 0x80
	s_addc_u32 s31, s31, 0
	s_add_u32 s58, s34, 0x100
	v_mov_b32_e32 v6, 0
	s_addc_u32 s59, s35, 0
	s_mov_b32 s34, 0
	v_mov_b32_e32 v7, v6
	v_mov_b32_e32 v8, v6
	v_mov_b32_e32 v9, v6
	v_mov_b32_e32 v14, v6
	v_mov_b32_e32 v15, v6
	v_mov_b32_e32 v16, v6
	v_mov_b32_e32 v17, v6
	v_mov_b32_e32 v26, v6
	v_mov_b32_e32 v27, v6
	v_mov_b32_e32 v28, v6
	v_mov_b32_e32 v29, v6
	v_mov_b32_e32 v30, v6
	v_mov_b32_e32 v31, v6
	v_mov_b32_e32 v32, v6
	v_mov_b32_e32 v33, v6
	v_mov_b32_e32 v42, v6
	v_mov_b32_e32 v43, v6
	v_mov_b32_e32 v44, v6
	v_mov_b32_e32 v45, v6
	v_mov_b32_e32 v46, v6
	v_mov_b32_e32 v47, v6
	v_mov_b32_e32 v48, v6
	v_mov_b32_e32 v49, v6
	v_mov_b32_e32 v58, v6
	v_mov_b32_e32 v59, v6
	v_mov_b32_e32 v60, v6
	v_mov_b32_e32 v61, v6
	v_mov_b32_e32 v62, v6
	v_mov_b32_e32 v63, v6
	v_mov_b32_e32 v64, v6
	v_mov_b32_e32 v65, v6
	v_mov_b32_e32 v66, v6
	v_mov_b32_e32 v67, v6
	v_mov_b32_e32 v68, v6
	v_mov_b32_e32 v69, v6
	v_mov_b32_e32 v70, v6
	v_mov_b32_e32 v71, v6
	v_mov_b32_e32 v72, v6
	v_mov_b32_e32 v73, v6
	v_mov_b32_e32 v82, v6
	v_mov_b32_e32 v83, v6
	v_mov_b32_e32 v84, v6
	v_mov_b32_e32 v85, v6
	v_mov_b32_e32 v86, v6
	v_mov_b32_e32 v87, v6
	v_mov_b32_e32 v88, v6
	v_mov_b32_e32 v89, v6
	v_mov_b32_e32 v98, v6
	v_mov_b32_e32 v99, v6
	v_mov_b32_e32 v100, v6
	v_mov_b32_e32 v101, v6
	v_mov_b32_e32 v102, v6
	v_mov_b32_e32 v103, v6
	v_mov_b32_e32 v104, v6
	v_mov_b32_e32 v105, v6
	v_mov_b32_e32 v114, v6
	v_mov_b32_e32 v115, v6
	v_mov_b32_e32 v116, v6
	v_mov_b32_e32 v117, v6
	v_mov_b32_e32 v118, v6
	v_mov_b32_e32 v119, v6
	v_mov_b32_e32 v120, v6
	v_mov_b32_e32 v121, v6
	v_mov_b32_e32 v74, v6
	v_mov_b32_e32 v75, v6
	v_mov_b32_e32 v76, v6
	v_mov_b32_e32 v77, v6
	v_mov_b32_e32 v78, v6
	v_mov_b32_e32 v79, v6
	v_mov_b32_e32 v80, v6
	v_mov_b32_e32 v81, v6
	v_mov_b32_e32 v90, v6
	v_mov_b32_e32 v91, v6
	v_mov_b32_e32 v92, v6
	v_mov_b32_e32 v93, v6
	v_mov_b32_e32 v94, v6
	v_mov_b32_e32 v95, v6
	v_mov_b32_e32 v96, v6
	v_mov_b32_e32 v97, v6
	v_mov_b32_e32 v106, v6
	v_mov_b32_e32 v107, v6
	v_mov_b32_e32 v108, v6
	v_mov_b32_e32 v109, v6
	v_mov_b32_e32 v110, v6
	v_mov_b32_e32 v111, v6
	v_mov_b32_e32 v112, v6
	v_mov_b32_e32 v113, v6
	v_mov_b32_e32 v122, v6
	v_mov_b32_e32 v123, v6
	v_mov_b32_e32 v124, v6
	v_mov_b32_e32 v125, v6
	v_mov_b32_e32 v126, v6
	v_mov_b32_e32 v127, v6
	v_mov_b32_e32 v128, v6
	v_mov_b32_e32 v129, v6
	v_mov_b32_e32 v54, v6
	v_mov_b32_e32 v55, v6
	v_mov_b32_e32 v56, v6
	v_mov_b32_e32 v57, v6
	v_mov_b32_e32 v50, v6
	v_mov_b32_e32 v51, v6
	v_mov_b32_e32 v52, v6
	v_mov_b32_e32 v53, v6
	v_mov_b32_e32 v38, v6
	v_mov_b32_e32 v39, v6
	v_mov_b32_e32 v40, v6
	v_mov_b32_e32 v41, v6
	v_mov_b32_e32 v34, v6
	v_mov_b32_e32 v35, v6
	v_mov_b32_e32 v36, v6
	v_mov_b32_e32 v37, v6
	v_mov_b32_e32 v22, v6
	v_mov_b32_e32 v23, v6
	v_mov_b32_e32 v24, v6
	v_mov_b32_e32 v25, v6
	v_mov_b32_e32 v18, v6
	v_mov_b32_e32 v19, v6
	v_mov_b32_e32 v20, v6
	v_mov_b32_e32 v21, v6
	v_mov_b32_e32 v10, v6
	v_mov_b32_e32 v11, v6
	v_mov_b32_e32 v12, v6
	v_mov_b32_e32 v13, v6
	v_mov_b32_e32 v2, v6
	v_mov_b32_e32 v3, v6
	v_mov_b32_e32 v4, v6
	v_mov_b32_e32 v5, v6

; template <class Epi, class Sched, bool ALIGN_EPI = false, bool SP2 = false>
; __device__ __forceinline__ void gemm_phase(PG8_LAS unsigned char* lds, const Gemm g, const Sched& S, const Epi& E) {
;     ...
;         for (int t = 0; t < nt; t += 2) {
;             if constexpr (Epi::MIDK) { if (t == (nt >> 1)) E.mid(acc, cur, wr, wc, fr, fq); }
;             const bool last = (t == nt - 2);
;             const char* a1 = cA + (size_t)(t + 1) * kstep;
;             const char* a2 = last ? nA : cA + (size_t)(t + 2) * kstep; const char* b2 = last ? nB : cB + (size_t)(t + 2) * kstep;
;             const char* a3 = a2 + kstep; const char* b3 = b2 + kstep;
;     ...
;         for (int a = 0; a < 2; ++a)
; #pragma unroll
;             for (int b = 0; b < 2; ++b)
; #pragma unroll
;                 for (int m = 0; m < 4; ++m)
; #pragma unroll
;                     for (int n = 0; n < 2; ++n) acc[a][b][m][n] = (f32x4){0.f, 0.f, 0.f, 0.f};
;         cur = nxt; cA = nA; cB = nB; ++ui;
.LBB0_1623:
	v_mov_b32_e32 v37, 0
	s_andn2_b64 vcc, exec, s[30:31]
	s_cbranch_vccz .Lzk_6
	v_mov_b32_e32 v36, v37
	v_mov_b32_e32 v35, v37
	v_mov_b32_e32 v34, v37
	v_mov_b32_e32 v41, v37
	v_mov_b32_e32 v40, v37
	v_mov_b32_e32 v39, v37
	v_mov_b32_e32 v38, v37
	v_mov_b32_e32 v53, v37
	v_mov_b32_e32 v52, v37
	v_mov_b32_e32 v51, v37
	v_mov_b32_e32 v50, v37
	v_mov_b32_e32 v57, v37
	v_mov_b32_e32 v56, v37
	v_mov_b32_e32 v55, v37
	v_mov_b32_e32 v54, v37
	v_mov_b32_e32 v69, v37
	v_mov_b32_e32 v68, v37
	v_mov_b32_e32 v67, v37
	v_mov_b32_e32 v66, v37
	v_mov_b32_e32 v73, v37
	v_mov_b32_e32 v72, v37
	v_mov_b32_e32 v71, v37
	v_mov_b32_e32 v70, v37
	v_mov_b32_e32 v85, v37
	v_mov_b32_e32 v84, v37
	v_mov_b32_e32 v83, v37
	v_mov_b32_e32 v82, v37
	v_mov_b32_e32 v89, v37
	v_mov_b32_e32 v88, v37
	v_mov_b32_e32 v87, v37
	v_mov_b32_e32 v86, v37
	v_mov_b32_e32 v161, v37
	v_mov_b32_e32 v160, v37
	v_mov_b32_e32 v159, v37
	v_mov_b32_e32 v158, v37
	v_mov_b32_e32 v157, v37
	v_mov_b32_e32 v156, v37
	v_mov_b32_e32 v155, v37
	v_mov_b32_e32 v154, v37
	v_mov_b32_e32 v145, v37
	v_mov_b32_e32 v144, v37
	v_mov_b32_e32 v143, v37
	v_mov_b32_e32 v142, v37
	v_mov_b32_e32 v141, v37
	v_mov_b32_e32 v140, v37
	v_mov_b32_e32 v139, v37
	v_mov_b32_e32 v138, v37
	v_mov_b32_e32 v129, v37
	v_mov_b32_e32 v128, v37
	v_mov_b32_e32 v127, v37
	v_mov_b32_e32 v126, v37
	v_mov_b32_e32 v125, v37
	v_mov_b32_e32 v124, v37
	v_mov_b32_e32 v123, v37
	v_mov_b32_e32 v122, v37
	v_mov_b32_e32 v113, v37
	v_mov_b32_e32 v112, v37
	v_mov_b32_e32 v111, v37
	v_mov_b32_e32 v110, v37
	v_mov_b32_e32 v109, v37
	v_mov_b32_e32 v108, v37
	v_mov_b32_e32 v107, v37
	v_mov_b32_e32 v106, v37
	v_mov_b32_e32 v153, v37
	v_mov_b32_e32 v152, v37
	v_mov_b32_e32 v151, v37
	v_mov_b32_e32 v150, v37
	v_mov_b32_e32 v149, v37
	v_mov_b32_e32 v148, v37
	v_mov_b32_e32 v147, v37
	v_mov_b32_e32 v146, v37
	v_mov_b32_e32 v137, v37
	v_mov_b32_e32 v136, v37
	v_mov_b32_e32 v135, v37
	v_mov_b32_e32 v134, v37
	v_mov_b32_e32 v133, v37
	v_mov_b32_e32 v132, v37
	v_mov_b32_e32 v131, v37
	v_mov_b32_e32 v130, v37
	v_mov_b32_e32 v121, v37
	v_mov_b32_e32 v120, v37
	v_mov_b32_e32 v119, v37
	v_mov_b32_e32 v118, v37
	v_mov_b32_e32 v117, v37
	v_mov_b32_e32 v116, v37
	v_mov_b32_e32 v115, v37
	v_mov_b32_e32 v114, v37
	v_mov_b32_e32 v105, v37
	v_mov_b32_e32 v104, v37
	v_mov_b32_e32 v103, v37
	v_mov_b32_e32 v102, v37
	v_mov_b32_e32 v101, v37
	v_mov_b32_e32 v100, v37
	v_mov_b32_e32 v99, v37
	v_mov_b32_e32 v98, v37
	v_mov_b32_e32 v97, v37
	v_mov_b32_e32 v96, v37
	v_mov_b32_e32 v95, v37
	v_mov_b32_e32 v94, v37
	v_mov_b32_e32 v93, v37
	v_mov_b32_e32 v92, v37
	v_mov_b32_e32 v91, v37
	v_mov_b32_e32 v90, v37
	v_mov_b32_e32 v81, v37
	v_mov_b32_e32 v80, v37
	v_mov_b32_e32 v79, v37
	v_mov_b32_e32 v78, v37
	v_mov_b32_e32 v77, v37
	v_mov_b32_e32 v76, v37
	v_mov_b32_e32 v75, v37
	v_mov_b32_e32 v74, v37
	v_mov_b32_e32 v65, v37
	v_mov_b32_e32 v64, v37
	v_mov_b32_e32 v63, v37
	v_mov_b32_e32 v62, v37
	v_mov_b32_e32 v61, v37
	v_mov_b32_e32 v60, v37
	v_mov_b32_e32 v59, v37
	v_mov_b32_e32 v58, v37
	v_mov_b32_e32 v49, v37
	v_mov_b32_e32 v48, v37
	v_mov_b32_e32 v47, v37
	v_mov_b32_e32 v46, v37
	v_mov_b32_e32 v45, v37
	v_mov_b32_e32 v44, v37
	v_mov_b32_e32 v43, v37
	v_mov_b32_e32 v42, v37
	s_branch .LBB0_1626
.Lzk_6:
	s_add_u32 s46, s46, 0x80
	s_addc_u32 s47, s47, 0
	s_add_u32 s80, s48, 0x100
	v_mov_b32_e32 v42, 0
	s_addc_u32 s81, s49, 0
	s_mov_b32 s48, 0
	v_mov_b32_e32 v43, v42
	v_mov_b32_e32 v44, v42
	v_mov_b32_e32 v45, v42
	v_mov_b32_e32 v46, v42
	v_mov_b32_e32 v47, v42
	v_mov_b32_e32 v48, v42
	v_mov_b32_e32 v49, v42
	v_mov_b32_e32 v58, v42
	v_mov_b32_e32 v59, v42
	v_mov_b32_e32 v60, v42
	v_mov_b32_e32 v61, v42
	v_mov_b32_e32 v62, v42
	v_mov_b32_e32 v63, v42
	v_mov_b32_e32 v64, v42
	v_mov_b32_e32 v65, v42
	v_mov_b32_e32 v74, v42
	v_mov_b32_e32 v75, v42
	v_mov_b32_e32 v76, v42
	v_mov_b32_e32 v77, v42
	v_mov_b32_e32 v78, v42
	v_mov_b32_e32 v79, v42
	v_mov_b32_e32 v80, v42
	v_mov_b32_e32 v81, v42
	v_mov_b32_e32 v90, v42
	v_mov_b32_e32 v91, v42
	v_mov_b32_e32 v92, v42
	v_mov_b32_e32 v93, v42
	v_mov_b32_e32 v94, v42
	v_mov_b32_e32 v95, v42
	v_mov_b32_e32 v96, v42
	v_mov_b32_e32 v97, v42
	v_mov_b32_e32 v98, v42
	v_mov_b32_e32 v99, v42
	v_mov_b32_e32 v100, v42
	v_mov_b32_e32 v101, v42
	v_mov_b32_e32 v102, v42
	v_mov_b32_e32 v103, v42
	v_mov_b32_e32 v104, v42
	v_mov_b32_e32 v105, v42
	v_mov_b32_e32 v114, v42
	v_mov_b32_e32 v115, v42
	v_mov_b32_e32 v116, v42
	v_mov_b32_e32 v117, v42
	v_mov_b32_e32 v118, v42
	v_mov_b32_e32 v119, v42
	v_mov_b32_e32 v120, v42
	v_mov_b32_e32 v121, v42
	v_mov_b32_e32 v130, v42
	v_mov_b32_e32 v131, v42
	v_mov_b32_e32 v132, v42
	v_mov_b32_e32 v133, v42
	v_mov_b32_e32 v134, v42
	v_mov_b32_e32 v135, v42
	v_mov_b32_e32 v136, v42
	v_mov_b32_e32 v137, v42
	v_mov_b32_e32 v146, v42
	v_mov_b32_e32 v147, v42
	v_mov_b32_e32 v148, v42
	v_mov_b32_e32 v149, v42
	v_mov_b32_e32 v150, v42
	v_mov_b32_e32 v151, v42
	v_mov_b32_e32 v152, v42
	v_mov_b32_e32 v153, v42
	v_mov_b32_e32 v106, v42
	v_mov_b32_e32 v107, v42
	v_mov_b32_e32 v108, v42
	v_mov_b32_e32 v109, v42
	v_mov_b32_e32 v110, v42
	v_mov_b32_e32 v111, v42
	v_mov_b32_e32 v112, v42
	v_mov_b32_e32 v113, v42
	v_mov_b32_e32 v122, v42
	v_mov_b32_e32 v123, v42
	v_mov_b32_e32 v124, v42
	v_mov_b32_e32 v125, v42
	v_mov_b32_e32 v126, v42
	v_mov_b32_e32 v127, v42
	v_mov_b32_e32 v128, v42
	v_mov_b32_e32 v129, v42
	v_mov_b32_e32 v138, v42
	v_mov_b32_e32 v139, v42
	v_mov_b32_e32 v140, v42
	v_mov_b32_e32 v141, v42
	v_mov_b32_e32 v142, v42
	v_mov_b32_e32 v143, v42
	v_mov_b32_e32 v144, v42
	v_mov_b32_e32 v145, v42
	v_mov_b32_e32 v154, v42
	v_mov_b32_e32 v155, v42
	v_mov_b32_e32 v156, v42
	v_mov_b32_e32 v157, v42
	v_mov_b32_e32 v158, v42
	v_mov_b32_e32 v159, v42
	v_mov_b32_e32 v160, v42
	v_mov_b32_e32 v161, v42
	v_mov_b32_e32 v86, v42
	v_mov_b32_e32 v87, v42
	v_mov_b32_e32 v88, v42
	v_mov_b32_e32 v89, v42
	v_mov_b32_e32 v82, v42
	v_mov_b32_e32 v83, v42
	v_mov_b32_e32 v84, v42
	v_mov_b32_e32 v85, v42
	v_mov_b32_e32 v70, v42
	v_mov_b32_e32 v71, v42
	v_mov_b32_e32 v72, v42
	v_mov_b32_e32 v73, v42
	v_mov_b32_e32 v66, v42
	v_mov_b32_e32 v67, v42
	v_mov_b32_e32 v68, v42
	v_mov_b32_e32 v69, v42
	v_mov_b32_e32 v54, v42
	v_mov_b32_e32 v55, v42
	v_mov_b32_e32 v56, v42
	v_mov_b32_e32 v57, v42
	v_mov_b32_e32 v50, v42
	v_mov_b32_e32 v51, v42
	v_mov_b32_e32 v52, v42
	v_mov_b32_e32 v53, v42
	v_mov_b32_e32 v38, v42
	v_mov_b32_e32 v39, v42
	v_mov_b32_e32 v40, v42
	v_mov_b32_e32 v41, v42
	v_mov_b32_e32 v34, v42
	v_mov_b32_e32 v35, v42
	v_mov_b32_e32 v36, v42
	v_mov_b32_e32 v37, v42

; template <class Epi, class Sched, bool ALIGN_EPI = false, bool SP2 = false>
; __device__ __forceinline__ void gemm_phase(PG8_LAS unsigned char* lds, const Gemm g, const Sched& S, const Epi& E) {
;     ...
;         for (int t = 0; t < nt; t += 2) {
;             if constexpr (Epi::MIDK) { if (t == (nt >> 1)) E.mid(acc, cur, wr, wc, fr, fq); }
;             const bool last = (t == nt - 2);
;             const char* a1 = cA + (size_t)(t + 1) * kstep;
;             const char* a2 = last ? nA : cA + (size_t)(t + 2) * kstep; const char* b2 = last ? nB : cB + (size_t)(t + 2) * kstep;
;             const char* a3 = a2 + kstep; const char* b3 = b2 + kstep;
;     ...
;         for (int a = 0; a < 2; ++a)
; #pragma unroll
;             for (int b = 0; b < 2; ++b)
; #pragma unroll
;                 for (int m = 0; m < 4; ++m)
; #pragma unroll
;                     for (int n = 0; n < 2; ++n) acc[a][b][m][n] = (f32x4){0.f, 0.f, 0.f, 0.f};
;         cur = nxt; cA = nA; cB = nB; ++ui;
.LBB0_1656:
	v_mov_b32_e32 v35, 0
	s_andn2_b64 vcc, exec, s[38:39]
	s_cbranch_vccz .Lzk_7
	v_mov_b32_e32 v34, v35
	v_mov_b32_e32 v33, v35
	v_mov_b32_e32 v32, v35
	v_mov_b32_e32 v39, v35
	v_mov_b32_e32 v38, v35
	v_mov_b32_e32 v37, v35
	v_mov_b32_e32 v36, v35
	v_mov_b32_e32 v51, v35
	v_mov_b32_e32 v50, v35
	v_mov_b32_e32 v49, v35
	v_mov_b32_e32 v48, v35
	v_mov_b32_e32 v55, v35
	v_mov_b32_e32 v54, v35
	v_mov_b32_e32 v53, v35
	v_mov_b32_e32 v52, v35
	v_mov_b32_e32 v67, v35
	v_mov_b32_e32 v66, v35
	v_mov_b32_e32 v65, v35
	v_mov_b32_e32 v64, v35
	v_mov_b32_e32 v71, v35
	v_mov_b32_e32 v70, v35
	v_mov_b32_e32 v69, v35
	v_mov_b32_e32 v68, v35
	v_mov_b32_e32 v83, v35
	v_mov_b32_e32 v82, v35
	v_mov_b32_e32 v81, v35
	v_mov_b32_e32 v80, v35
	v_mov_b32_e32 v87, v35
	v_mov_b32_e32 v86, v35
	v_mov_b32_e32 v85, v35
	v_mov_b32_e32 v84, v35
	v_mov_b32_e32 v167, v35
	v_mov_b32_e32 v166, v35
	v_mov_b32_e32 v165, v35
	v_mov_b32_e32 v164, v35
	v_mov_b32_e32 v163, v35
	v_mov_b32_e32 v162, v35
	v_mov_b32_e32 v161, v35
	v_mov_b32_e32 v160, v35
	v_mov_b32_e32 v143, v35
	v_mov_b32_e32 v142, v35
	v_mov_b32_e32 v141, v35
	v_mov_b32_e32 v140, v35
	v_mov_b32_e32 v139, v35
	v_mov_b32_e32 v138, v35
	v_mov_b32_e32 v137, v35
	v_mov_b32_e32 v136, v35
	v_mov_b32_e32 v111, v35
	v_mov_b32_e32 v110, v35
	v_mov_b32_e32 v109, v35
	v_mov_b32_e32 v108, v35
	v_mov_b32_e32 v107, v35
	v_mov_b32_e32 v106, v35
	v_mov_b32_e32 v105, v35
	v_mov_b32_e32 v104, v35
	v_mov_b32_e32 v119, v35
	v_mov_b32_e32 v118, v35
	v_mov_b32_e32 v117, v35
	v_mov_b32_e32 v116, v35
	v_mov_b32_e32 v115, v35
	v_mov_b32_e32 v114, v35
	v_mov_b32_e32 v113, v35
	v_mov_b32_e32 v112, v35
	v_mov_b32_e32 v151, v35
	v_mov_b32_e32 v150, v35
	v_mov_b32_e32 v149, v35
	v_mov_b32_e32 v148, v35
	v_mov_b32_e32 v147, v35
	v_mov_b32_e32 v146, v35
	v_mov_b32_e32 v145, v35
	v_mov_b32_e32 v144, v35
	v_mov_b32_e32 v135, v35
	v_mov_b32_e32 v134, v35
	v_mov_b32_e32 v133, v35
	v_mov_b32_e32 v132, v35
	v_mov_b32_e32 v131, v35
	v_mov_b32_e32 v130, v35
	v_mov_b32_e32 v129, v35
	v_mov_b32_e32 v128, v35
	v_mov_b32_e32 v127, v35
	v_mov_b32_e32 v126, v35
	v_mov_b32_e32 v125, v35
	v_mov_b32_e32 v124, v35
	v_mov_b32_e32 v123, v35
	v_mov_b32_e32 v122, v35
	v_mov_b32_e32 v121, v35
	v_mov_b32_e32 v120, v35
	v_mov_b32_e32 v103, v35
	v_mov_b32_e32 v102, v35
	v_mov_b32_e32 v101, v35
	v_mov_b32_e32 v100, v35
	v_mov_b32_e32 v99, v35
	v_mov_b32_e32 v98, v35
	v_mov_b32_e32 v97, v35
	v_mov_b32_e32 v96, v35
	v_mov_b32_e32 v95, v35
	v_mov_b32_e32 v94, v35
	v_mov_b32_e32 v93, v35
	v_mov_b32_e32 v92, v35
	v_mov_b32_e32 v91, v35
	v_mov_b32_e32 v90, v35
	v_mov_b32_e32 v89, v35
	v_mov_b32_e32 v88, v35
	v_mov_b32_e32 v79, v35
	v_mov_b32_e32 v78, v35
	v_mov_b32_e32 v77, v35
	v_mov_b32_e32 v76, v35
	v_mov_b32_e32 v75, v35
	v_mov_b32_e32 v74, v35
	v_mov_b32_e32 v73, v35
	v_mov_b32_e32 v72, v35
	v_mov_b32_e32 v63, v35
	v_mov_b32_e32 v62, v35
	v_mov_b32_e32 v61, v35
	v_mov_b32_e32 v60, v35
	v_mov_b32_e32 v59, v35
	v_mov_b32_e32 v58, v35
	v_mov_b32_e32 v57, v35
	v_mov_b32_e32 v56, v35
	v_mov_b32_e32 v47, v35
	v_mov_b32_e32 v46, v35
	v_mov_b32_e32 v45, v35
	v_mov_b32_e32 v44, v35
	v_mov_b32_e32 v43, v35
	v_mov_b32_e32 v42, v35
	v_mov_b32_e32 v41, v35
	v_mov_b32_e32 v40, v35
	s_branch .LBB0_1659
.Lzk_7:
	s_add_u32 s2, s80, 0x80
	s_addc_u32 s3, s81, 0
	s_add_u32 s57, s78, 0x100
	v_mov_b32_e32 v40, 0
	s_addc_u32 s82, s79, 0
	s_mov_b32 s78, 0
	v_mov_b32_e32 v41, v40
	v_mov_b32_e32 v42, v40
	v_mov_b32_e32 v43, v40
	v_mov_b32_e32 v44, v40
	v_mov_b32_e32 v45, v40
	v_mov_b32_e32 v46, v40
	v_mov_b32_e32 v47, v40
	v_mov_b32_e32 v56, v40
	v_mov_b32_e32 v57, v40
	v_mov_b32_e32 v58, v40
	v_mov_b32_e32 v59, v40
	v_mov_b32_e32 v60, v40
	v_mov_b32_e32 v61, v40
	v_mov_b32_e32 v62, v40
	v_mov_b32_e32 v63, v40
	v_mov_b32_e32 v72, v40
	v_mov_b32_e32 v73, v40
	v_mov_b32_e32 v74, v40
	v_mov_b32_e32 v75, v40
	v_mov_b32_e32 v76, v40
	v_mov_b32_e32 v77, v40
	v_mov_b32_e32 v78, v40
	v_mov_b32_e32 v79, v40
	v_mov_b32_e32 v88, v40
	v_mov_b32_e32 v89, v40
	v_mov_b32_e32 v90, v40
	v_mov_b32_e32 v91, v40
	v_mov_b32_e32 v92, v40
	v_mov_b32_e32 v93, v40
	v_mov_b32_e32 v94, v40
	v_mov_b32_e32 v95, v40
	v_mov_b32_e32 v96, v40
	v_mov_b32_e32 v97, v40
	v_mov_b32_e32 v98, v40
	v_mov_b32_e32 v99, v40
	v_mov_b32_e32 v100, v40
	v_mov_b32_e32 v101, v40
	v_mov_b32_e32 v102, v40
	v_mov_b32_e32 v103, v40
	v_mov_b32_e32 v120, v40
	v_mov_b32_e32 v121, v40
	v_mov_b32_e32 v122, v40
	v_mov_b32_e32 v123, v40
	v_mov_b32_e32 v124, v40
	v_mov_b32_e32 v125, v40
	v_mov_b32_e32 v126, v40
	v_mov_b32_e32 v127, v40
	v_mov_b32_e32 v128, v40
	v_mov_b32_e32 v129, v40
	v_mov_b32_e32 v130, v40
	v_mov_b32_e32 v131, v40
	v_mov_b32_e32 v132, v40
	v_mov_b32_e32 v133, v40
	v_mov_b32_e32 v134, v40
	v_mov_b32_e32 v135, v40
	v_mov_b32_e32 v144, v40
	v_mov_b32_e32 v145, v40
	v_mov_b32_e32 v146, v40
	v_mov_b32_e32 v147, v40
	v_mov_b32_e32 v148, v40
	v_mov_b32_e32 v149, v40
	v_mov_b32_e32 v150, v40
	v_mov_b32_e32 v151, v40
	v_mov_b32_e32 v112, v40
	v_mov_b32_e32 v113, v40
	v_mov_b32_e32 v114, v40
	v_mov_b32_e32 v115, v40
	v_mov_b32_e32 v116, v40
	v_mov_b32_e32 v117, v40
	v_mov_b32_e32 v118, v40
	v_mov_b32_e32 v119, v40
	v_mov_b32_e32 v104, v40
	v_mov_b32_e32 v105, v40
	v_mov_b32_e32 v106, v40
	v_mov_b32_e32 v107, v40
	v_mov_b32_e32 v108, v40
	v_mov_b32_e32 v109, v40
	v_mov_b32_e32 v110, v40
	v_mov_b32_e32 v111, v40
	v_mov_b32_e32 v136, v40
	v_mov_b32_e32 v137, v40
	v_mov_b32_e32 v138, v40
	v_mov_b32_e32 v139, v40
	v_mov_b32_e32 v140, v40
	v_mov_b32_e32 v141, v40
	v_mov_b32_e32 v142, v40
	v_mov_b32_e32 v143, v40
	v_mov_b32_e32 v160, v40
	v_mov_b32_e32 v161, v40
	v_mov_b32_e32 v162, v40
	v_mov_b32_e32 v163, v40
	v_mov_b32_e32 v164, v40
	v_mov_b32_e32 v165, v40
	v_mov_b32_e32 v166, v40
	v_mov_b32_e32 v167, v40
	v_mov_b32_e32 v84, v40
	v_mov_b32_e32 v85, v40
	v_mov_b32_e32 v86, v40
	v_mov_b32_e32 v87, v40
	v_mov_b32_e32 v80, v40
	v_mov_b32_e32 v81, v40
	v_mov_b32_e32 v82, v40
	v_mov_b32_e32 v83, v40
	v_mov_b32_e32 v68, v40
	v_mov_b32_e32 v69, v40
	v_mov_b32_e32 v70, v40
	v_mov_b32_e32 v71, v40
	v_mov_b32_e32 v64, v40
	v_mov_b32_e32 v65, v40
	v_mov_b32_e32 v66, v40
	v_mov_b32_e32 v67, v40
	v_mov_b32_e32 v52, v40
	v_mov_b32_e32 v53, v40
	v_mov_b32_e32 v54, v40
	v_mov_b32_e32 v55, v40
	v_mov_b32_e32 v48, v40
	v_mov_b32_e32 v49, v40
	v_mov_b32_e32 v50, v40
	v_mov_b32_e32 v51, v40
	v_mov_b32_e32 v36, v40
	v_mov_b32_e32 v37, v40
	v_mov_b32_e32 v38, v40
	v_mov_b32_e32 v39, v40
	v_mov_b32_e32 v32, v40
	v_mov_b32_e32 v33, v40
	v_mov_b32_e32 v34, v40
	v_mov_b32_e32 v35, v40
